# v6 + grid barrier: agent acquire (buffer_inv sc1) issued by wave 1 at arrival instead of by leader after release
# speedup vs baseline: 1.0086x; 1.0064x over previous
; __device__ __forceinline__ unsigned xb_ld(unsigned* p)              { return __hip_atomic_load(p, __ATOMIC_RELAXED, __HIP_MEMORY_SCOPE_AGENT); }
; __device__ __forceinline__ void xcd_barrier_complete(unsigned* bar, unsigned x, unsigned& nloc, unsigned& nx) {
;     const unsigned G = gridDim.x * gridDim.y * gridDim.z;
;     unsigned sum, cnt, mine, sp = 0u;
;     for (;;) {
;         sum = 0u; cnt = 0u; mine = 0u;
; #pragma unroll
;         for (unsigned j = 0; j < 16; ++j) { const unsigned c = xb_ld(&bar[XB_XCNT(j)]); sum += c; cnt += (c > 0u) ? 1u : 0u; mine = (j == x) ? c : mine; }
; __device__ __forceinline__ void xcd_barrier(const XcdBarrier& b, bool leader) {
;     asm volatile("s_waitcnt vmcnt(0)" ::: "memory");
;     __syncthreads();
;     if (leader) {
;         unsigned zo_; asm volatile("v_mov_b32 %0, 0" : "=v"(zo_)); unsigned* bar = b.bar + zo_;
;         __builtin_amdgcn_s_waitcnt(0);
;         unsigned nloc = b.st[0], nx = b.st[1];
;         if (nloc == 0u) { xcd_barrier_complete(bar, b.x, nloc, nx); b.st[0] = nloc; b.st[1] = nx; }
.LBB0_196:
	s_or_b64 exec, exec, s[4:5]
	s_waitcnt lgkmcnt(0)
	s_mov_b64 s[2:3], s[88:89]
	s_mov_b32 s1, -1
	s_getreg_b32 s0, hwreg(HW_REG_XCC_ID, 0, 4)
	s_nop 0
	v_mbcnt_lo_u32_b32 v0, s1, 0
	v_mbcnt_hi_u32_b32 v0, s1, v0
	v_add_u32_e32 v0, s93, v0
	s_waitcnt vmcnt(0)
	s_nop 0
	v_cmp_eq_u32_e32 vcc, 0, v0
	s_barrier
	s_cmp_lg_u32 s93, 64
	s_cbranch_scc1 .Lbinv_skip_0
	buffer_inv sc1
	s_waitcnt vmcnt(0)
.Lbinv_skip_0:
	s_and_saveexec_b64 s[4:5], vcc
	v_writelane_b32 v255, s94, 29
	s_xor_b64 s[10:11], exec, s[4:5]
	s_nop 0
	v_writelane_b32 v255, s95, 30
	s_cbranch_execz .LBB0_241
	s_add_i32 s1, 0, 0x20020
	v_mov_b32_e32 v2, s1
	s_load_dwordx2 s[2:3], s[2:3], 0xf8
	v_mov_b32 v0, 0
	s_waitcnt vmcnt(0) expcnt(0) lgkmcnt(0)
	ds_read_b32 v6, v2
	s_add_i32 s1, 0, 0x20024
	v_mov_b32_e32 v2, s1
	ds_read_b32 v4, v2
	v_mov_b32_e32 v1, 0
	v_lshl_add_u64 v[0:1], v[0:1], 2, s[2:3]
	s_mov_b64 s[2:3], 0x4000
	s_waitcnt lgkmcnt(1)
	v_cmp_ne_u32_e32 vcc, 0, v6
	s_and_b32 s0, s0, 15
	v_lshl_add_u64 v[0:1], v[0:1], 0, s[2:3]
	s_cbranch_vccnz .LBB0_211
	v_readlane_b32 s4, v255, 0
	v_readlane_b32 s5, v255, 1
	s_load_dwordx2 s[2:3], s[4:5], 0x4
	s_mov_b64 s[4:5], 0x1000
	v_lshl_add_u64 v[2:3], v[0:1], 0, s[4:5]
	s_mov_b32 s22, 1
	s_waitcnt lgkmcnt(0)
	s_mul_i32 s1, s2, s60
	s_mul_i32 s1, s1, s3
	s_mov_b64 s[2:3], 0x1100
	v_lshl_add_u64 v[4:5], v[0:1], 0, s[2:3]
	s_mov_b64 s[2:3], 0x1200
	v_lshl_add_u64 v[6:7], v[0:1], 0, s[2:3]
	s_mov_b64 s[2:3], 0x1300
	v_lshl_add_u64 v[8:9], v[0:1], 0, s[2:3]
	s_mov_b64 s[2:3], 0
	s_branch .LBB0_201

; __device__ __forceinline__ unsigned xb_ld(unsigned* p)              { return __hip_atomic_load(p, __ATOMIC_RELAXED, __HIP_MEMORY_SCOPE_AGENT); }
; #define XB_SPIN(cond, bar) do { unsigned _sp = 0; while (cond) { __builtin_amdgcn_s_sleep(1); \
;     if ((++_sp & 255u) == 0u) { if (xb_ld(&(bar)[XB_TMO])) break; if (_sp > XB_SPIN_CAP) { atomicAdd(&(bar)[XB_TMO], 1u); break; } } } } while (0)
; __device__ __forceinline__ void xcd_barrier(const XcdBarrier& b, bool leader) {
;     ...
;             XB_SPIN(xb_ld(&bar[XB_XGEN(b.x)]) == gen, bar);
;             __builtin_amdgcn_fence(__ATOMIC_ACQUIRE, "agent");
;             asm volatile("s_waitcnt vmcnt(0)" ::: "memory");
.LBB0_223:
	s_or_b64 exec, exec, s[4:5]
	s_waitcnt vmcnt(0)
	s_nop 0
	s_waitcnt vmcnt(0)

; __device__ __forceinline__ unsigned xb_add(unsigned* p, unsigned v) { return __hip_atomic_fetch_add(p, v, __ATOMIC_RELAXED, __HIP_MEMORY_SCOPE_AGENT); }
; __device__ __forceinline__ void xcd_barrier(const XcdBarrier& b, bool leader) {
;     ...
;             __builtin_amdgcn_fence(__ATOMIC_ACQUIRE, "agent");
;             xb_add(&bar[XB_XGEN(b.x)], 1u);
;             asm volatile("s_waitcnt vmcnt(0)" ::: "memory");
.LBB0_239:
	s_or_b64 exec, exec, s[4:5]
	v_add_co_u32_e32 v0, vcc, 0x2000, v2
	v_mov_b32_e32 v2, 1
	s_nop 0
	v_addc_co_u32_e32 v1, vcc, 0, v3, vcc
	s_waitcnt vmcnt(0)
	s_nop 0
	global_atomic_add v[0:1], v2, off offset:1024
	s_waitcnt vmcnt(0)

; __device__ __forceinline__ unsigned xb_ld(unsigned* p)              { return __hip_atomic_load(p, __ATOMIC_RELAXED, __HIP_MEMORY_SCOPE_AGENT); }
; __device__ __forceinline__ unsigned xb_add(unsigned* p, unsigned v) { return __hip_atomic_fetch_add(p, v, __ATOMIC_RELAXED, __HIP_MEMORY_SCOPE_AGENT); }
; #define XB_SPIN(cond, bar) do { unsigned _sp = 0; while (cond) { __builtin_amdgcn_s_sleep(1); \
;     if ((++_sp & 255u) == 0u) { if (xb_ld(&(bar)[XB_TMO])) break; if (_sp > XB_SPIN_CAP) { atomicAdd(&(bar)[XB_TMO], 1u); break; } } } } while (0)
; __device__ __forceinline__ void xcd_barrier(const XcdBarrier& b, bool leader) {
;     ...
;             if (og + 1u == (tg + 1u) * nx) xb_add(&bar[XB_TOPGEN], 1u);
;             else XB_SPIN(xb_ld(&bar[XB_TOPGEN]) == tg, bar);
;             __builtin_amdgcn_fence(__ATOMIC_ACQUIRE, "agent");
;             xb_add(&bar[XB_XGEN(b.x)], 1u);
;             asm volatile("s_waitcnt vmcnt(0)" ::: "memory");
.LBB0_242:
	s_or_b64 exec, exec, s[2:3]
	v_add_co_u32_e32 v0, vcc, 0x2000, v2
	s_waitcnt vmcnt(0)
	s_nop 0
	v_addc_co_u32_e32 v1, vcc, 0, v3, vcc
	global_atomic_add v[0:1], v231, off offset:1024
	s_waitcnt vmcnt(0)

; __device__ __forceinline__ void xcd_barrier(const XcdBarrier& b, bool leader) {
;     asm volatile("s_waitcnt vmcnt(0)" ::: "memory");
;     __syncthreads();
;     if (leader) {
;         unsigned zo_; asm volatile("v_mov_b32 %0, 0" : "=v"(zo_)); unsigned* bar = b.bar + zo_;
;         __builtin_amdgcn_s_waitcnt(0);
;         unsigned nloc = b.st[0], nx = b.st[1];
;         if (nloc == 0u) { xcd_barrier_complete(bar, b.x, nloc, nx); b.st[0] = nloc; b.st[1] = nx; }
.LBB0_458:
	s_mov_b64 s[2:3], s[88:89]
	s_mov_b32 s4, s38
	s_getreg_b32 s1, hwreg(HW_REG_XCC_ID, 0, 4)
	s_nop 0
	v_mbcnt_lo_u32_b32 v0, s4, 0
	v_mbcnt_hi_u32_b32 v0, s4, v0
	v_add_u32_e32 v0, s93, v0
	s_waitcnt vmcnt(0)
	s_waitcnt vmcnt(16)
	v_cmp_eq_u32_e32 vcc, 0, v0
	s_barrier
	s_cmp_lg_u32 s93, 64
	s_cbranch_scc1 .Lbinv_skip_1
	buffer_inv sc1
	s_waitcnt vmcnt(0)
.Lbinv_skip_1:
	s_and_saveexec_b64 s[4:5], vcc
	s_xor_b64 s[10:11], exec, s[4:5]
	s_cbranch_execz .LBB0_503
	s_load_dwordx2 s[2:3], s[2:3], 0xf8
	v_mov_b32 v232, 0
	s_waitcnt vmcnt(0) expcnt(0) lgkmcnt(0)
	s_and_b32 s1, s1, 15
	v_lshl_add_u64 v[0:1], v[232:233], 2, s[2:3]
	s_mov_b64 s[2:3], 0x4000
	v_lshl_add_u64 v[0:1], v[0:1], 0, s[2:3]
	v_readlane_b32 s2, v255, 7
	s_nop 1
	v_mov_b32_e32 v2, s2
	ds_read_b32 v6, v2
	v_readlane_b32 s2, v255, 8
	s_waitcnt lgkmcnt(0)
	v_cmp_ne_u32_e32 vcc, 0, v6
	v_mov_b32_e32 v2, s2
	ds_read_b32 v4, v2
	s_cbranch_vccnz .LBB0_473
	v_readlane_b32 s4, v255, 0
	v_readlane_b32 s5, v255, 1
	s_load_dwordx2 s[2:3], s[4:5], 0x4
	s_mov_b64 s[4:5], 0x1100
	s_waitcnt lgkmcnt(0)
	v_lshl_add_u64 v[4:5], v[0:1], 0, s[4:5]
	s_mov_b64 s[4:5], 0x1200
	v_lshl_add_u64 v[6:7], v[0:1], 0, s[4:5]
	s_mov_b64 s[4:5], 0x1300
	v_lshl_add_u64 v[8:9], v[0:1], 0, s[4:5]
	v_readlane_b32 s4, v255, 4
	s_mul_i32 s22, s2, s4
	v_lshl_add_u64 v[2:3], v[0:1], 0, s[72:73]
	v_readlane_b32 s5, v255, 5
	s_mul_i32 s22, s22, s3
	s_mov_b32 s23, 1
	s_mov_b64 s[2:3], 0
	s_branch .LBB0_463

; __device__ __forceinline__ unsigned xb_add(unsigned* p, unsigned v) { return __hip_atomic_fetch_add(p, v, __ATOMIC_RELAXED, __HIP_MEMORY_SCOPE_AGENT); }
; __device__ __forceinline__ void xcd_barrier(const XcdBarrier& b, bool leader) {
;     ...
;             __builtin_amdgcn_fence(__ATOMIC_ACQUIRE, "agent");
;             xb_add(&bar[XB_XGEN(b.x)], 1u);
;             asm volatile("s_waitcnt vmcnt(0)" ::: "memory");
.LBB0_501:
	s_or_b64 exec, exec, s[4:5]
	v_add_co_u32_e32 v0, vcc, 0x2000, v2
	s_waitcnt vmcnt(0)
	s_nop 0
	v_addc_co_u32_e32 v1, vcc, 0, v3, vcc
	global_atomic_add v[0:1], v231, off offset:1024
	s_waitcnt vmcnt(0)

; __device__ __forceinline__ void xcd_barrier(const XcdBarrier& b, bool leader) {
;     asm volatile("s_waitcnt vmcnt(0)" ::: "memory");
;     __syncthreads();
;     if (leader) {
;         unsigned zo_; asm volatile("v_mov_b32 %0, 0" : "=v"(zo_)); unsigned* bar = b.bar + zo_;
;         __builtin_amdgcn_s_waitcnt(0);
;         unsigned nloc = b.st[0], nx = b.st[1];
;         if (nloc == 0u) { xcd_barrier_complete(bar, b.x, nloc, nx); b.st[0] = nloc; b.st[1] = nx; }
.LBB0_679:
	s_mov_b64 s[2:3], s[88:89]
	s_mov_b32 s4, s38
	s_getreg_b32 s1, hwreg(HW_REG_XCC_ID, 0, 4)
	s_nop 0
	v_mbcnt_lo_u32_b32 v0, s4, 0
	v_mbcnt_hi_u32_b32 v0, s4, v0
	v_add_u32_e32 v0, s93, v0
	s_waitcnt vmcnt(0)
	s_nop 0
	v_cmp_eq_u32_e32 vcc, 0, v0
	s_barrier
	s_cmp_lg_u32 s93, 64
	s_cbranch_scc1 .Lbinv_skip_2
	buffer_inv sc1
	s_waitcnt vmcnt(0)
.Lbinv_skip_2:
	s_and_saveexec_b64 s[36:37], vcc
	s_cbranch_execz .LBB0_723
	s_load_dwordx2 s[2:3], s[2:3], 0xf8
	v_mov_b32 v232, 0
	s_waitcnt vmcnt(0) expcnt(0) lgkmcnt(0)
	s_and_b32 s1, s1, 15
	v_lshl_add_u64 v[0:1], v[232:233], 2, s[2:3]
	s_mov_b64 s[2:3], 0x4000
	v_lshl_add_u64 v[0:1], v[0:1], 0, s[2:3]
	v_readlane_b32 s2, v255, 7
	s_nop 1
	v_mov_b32_e32 v2, s2
	ds_read_b32 v6, v2
	v_readlane_b32 s2, v255, 8
	s_waitcnt lgkmcnt(0)
	v_cmp_ne_u32_e32 vcc, 0, v6
	v_mov_b32_e32 v2, s2
	ds_read_b32 v4, v2
	s_cbranch_vccnz .LBB0_694
	v_readlane_b32 s4, v255, 0
	v_readlane_b32 s5, v255, 1
	s_load_dwordx2 s[2:3], s[4:5], 0x4
	s_mov_b64 s[4:5], 0x1100
	s_waitcnt lgkmcnt(0)
	v_lshl_add_u64 v[4:5], v[0:1], 0, s[4:5]
	s_mov_b64 s[4:5], 0x1200
	v_lshl_add_u64 v[6:7], v[0:1], 0, s[4:5]
	s_mov_b64 s[4:5], 0x1300
	v_lshl_add_u64 v[8:9], v[0:1], 0, s[4:5]
	v_readlane_b32 s4, v255, 4
	s_mul_i32 s20, s2, s4
	v_lshl_add_u64 v[2:3], v[0:1], 0, s[72:73]
	v_readlane_b32 s5, v255, 5
	s_mul_i32 s20, s20, s3
	s_mov_b32 s21, 1
	s_mov_b64 s[2:3], 0
	s_branch .LBB0_684

; __device__ __forceinline__ void xcd_barrier(const XcdBarrier& b, bool leader) {
;     asm volatile("s_waitcnt vmcnt(0)" ::: "memory");
;     __syncthreads();
;     if (leader) {
.LBB0_1060:
	s_waitcnt lgkmcnt(0)
	s_mov_b64 s[2:3], s[88:89]
	s_mov_b32 s4, s38
	s_getreg_b32 s1, hwreg(HW_REG_XCC_ID, 0, 4)
	s_nop 0
	v_mbcnt_lo_u32_b32 v0, s4, 0
	v_mbcnt_hi_u32_b32 v0, s4, v0
	v_add_u32_e32 v0, s93, v0
	s_waitcnt vmcnt(0)
	s_nop 0
	v_cmp_eq_u32_e32 vcc, 0, v0
	s_barrier
	s_cmp_lg_u32 s93, 64
	s_cbranch_scc1 .Lbinv_skip_5
	buffer_inv sc1
	s_waitcnt vmcnt(0)

; __device__ __forceinline__ void xcd_barrier(const XcdBarrier& b, bool leader) {
;     asm volatile("s_waitcnt vmcnt(0)" ::: "memory");
;     __syncthreads();
;     if (leader) {
.LBB0_1372:
	s_mov_b64 s[2:3], s[88:89]
	s_mov_b32 s4, s38
	s_getreg_b32 s1, hwreg(HW_REG_XCC_ID, 0, 4)
	s_nop 0
	v_mbcnt_lo_u32_b32 v0, s4, 0
	v_mbcnt_hi_u32_b32 v0, s4, v0
	v_add_u32_e32 v0, s93, v0
	s_waitcnt vmcnt(0)
	s_waitcnt vmcnt(8)
	v_cmp_eq_u32_e32 vcc, 0, v0
	s_barrier
	s_cmp_lg_u32 s93, 64
	s_cbranch_scc1 .Lbinv_skip_8
	buffer_inv sc1
	s_waitcnt vmcnt(0)

; __device__ __forceinline__ void xcd_barrier(const XcdBarrier& b, bool leader) {
;     ...
;     if (leader) {
;         unsigned zo_; asm volatile("v_mov_b32 %0, 0" : "=v"(zo_)); unsigned* bar = b.bar + zo_;
;         __builtin_amdgcn_s_waitcnt(0);
;         unsigned nloc = b.st[0], nx = b.st[1];
;         if (nloc == 0u) { xcd_barrier_complete(bar, b.x, nloc, nx); b.st[0] = nloc; b.st[1] = nx; }
.Lbinv_skip_10:
	s_and_saveexec_b64 s[10:11], vcc
	s_cbranch_execz .LBB0_1615
	s_load_dwordx2 s[2:3], s[2:3], 0xf8
	v_mov_b32 v232, 0
	s_waitcnt vmcnt(0) expcnt(0) lgkmcnt(0)
	s_and_b32 s1, s1, 15
	v_lshl_add_u64 v[0:1], v[232:233], 2, s[2:3]
	s_mov_b64 s[2:3], 0x4000
	v_lshl_add_u64 v[0:1], v[0:1], 0, s[2:3]
	v_readlane_b32 s2, v255, 7
	s_nop 1
	v_mov_b32_e32 v2, s2
	ds_read_b32 v6, v2
	v_readlane_b32 s2, v255, 8
	s_waitcnt lgkmcnt(0)
	v_cmp_ne_u32_e32 vcc, 0, v6
	v_mov_b32_e32 v2, s2
	ds_read_b32 v4, v2
	s_cbranch_vccnz .LBB0_1586
	v_readlane_b32 s4, v255, 0
	v_readlane_b32 s5, v255, 1
	s_load_dwordx2 s[2:3], s[4:5], 0x4
	s_mov_b64 s[4:5], 0x1100
	s_waitcnt lgkmcnt(0)
	v_lshl_add_u64 v[4:5], v[0:1], 0, s[4:5]
	s_mov_b64 s[4:5], 0x1200
	v_lshl_add_u64 v[6:7], v[0:1], 0, s[4:5]
	s_mov_b64 s[4:5], 0x1300
	v_lshl_add_u64 v[8:9], v[0:1], 0, s[4:5]
	v_readlane_b32 s4, v255, 4
	s_mul_i32 s22, s2, s4
	v_lshl_add_u64 v[2:3], v[0:1], 0, s[72:73]
	v_readlane_b32 s5, v255, 5
	s_mul_i32 s22, s22, s3
	s_mov_b32 s23, 1
	s_mov_b64 s[2:3], 0
	s_branch .LBB0_1576

; __device__ __forceinline__ void xcd_barrier(const XcdBarrier& b, bool leader) {
;     asm volatile("s_waitcnt vmcnt(0)" ::: "memory");
;     __syncthreads();
;     if (leader) {
;         unsigned zo_; asm volatile("v_mov_b32 %0, 0" : "=v"(zo_)); unsigned* bar = b.bar + zo_;
;         __builtin_amdgcn_s_waitcnt(0);
;         unsigned nloc = b.st[0], nx = b.st[1];
;         if (nloc == 0u) { xcd_barrier_complete(bar, b.x, nloc, nx); b.st[0] = nloc; b.st[1] = nx; }
.LBB0_1636:
	s_mov_b64 s[2:3], s[88:89]
	s_mov_b32 s5, s38
	s_getreg_b32 s4, hwreg(HW_REG_XCC_ID, 0, 4)
	s_nop 0
	v_mbcnt_lo_u32_b32 v0, s5, 0
	v_mbcnt_hi_u32_b32 v0, s5, v0
	v_add_u32_e32 v0, s93, v0
	s_waitcnt vmcnt(0)
	s_nop 0
	v_cmp_eq_u32_e32 vcc, 0, v0
	s_barrier
	s_cmp_lg_u32 s93, 64
	s_cbranch_scc1 .Lbinv_skip_11
	buffer_inv sc1
	s_waitcnt vmcnt(0)
.Lbinv_skip_11:
	s_and_saveexec_b64 s[6:7], vcc
	s_xor_b64 s[10:11], exec, s[6:7]
	s_cbranch_execz .LBB0_1681
	s_load_dwordx2 s[2:3], s[2:3], 0xf8
	v_mov_b32 v232, 0
	s_waitcnt vmcnt(0) expcnt(0) lgkmcnt(0)
	s_and_b32 s33, s4, 15
	v_lshl_add_u64 v[0:1], v[232:233], 2, s[2:3]
	s_mov_b64 s[2:3], 0x4000
	v_lshl_add_u64 v[0:1], v[0:1], 0, s[2:3]
	v_readlane_b32 s2, v255, 7
	s_nop 1
	v_mov_b32_e32 v2, s2
	ds_read_b32 v6, v2
	v_readlane_b32 s2, v255, 8
	s_waitcnt lgkmcnt(0)
	v_cmp_ne_u32_e32 vcc, 0, v6
	v_mov_b32_e32 v2, s2
	ds_read_b32 v4, v2
	s_cbranch_vccnz .LBB0_1651
	v_readlane_b32 s4, v255, 0
	v_readlane_b32 s5, v255, 1
	s_load_dwordx2 s[2:3], s[4:5], 0x4
	s_mov_b64 s[4:5], 0x1100
	s_waitcnt lgkmcnt(0)
	v_lshl_add_u64 v[4:5], v[0:1], 0, s[4:5]
	s_mov_b64 s[4:5], 0x1200
	v_lshl_add_u64 v[6:7], v[0:1], 0, s[4:5]
	s_mov_b64 s[4:5], 0x1300
	v_lshl_add_u64 v[8:9], v[0:1], 0, s[4:5]
	v_readlane_b32 s4, v255, 4
	s_mul_i32 s22, s2, s4
	v_lshl_add_u64 v[2:3], v[0:1], 0, s[72:73]
	v_readlane_b32 s5, v255, 5
	s_mul_i32 s22, s22, s3
	s_mov_b32 s23, 1
	s_mov_b64 s[2:3], 0
	s_branch .LBB0_1641

; __device__ __forceinline__ void xcd_barrier(const XcdBarrier& b, bool leader) {
;     asm volatile("s_waitcnt vmcnt(0)" ::: "memory");
;     __syncthreads();
;     if (leader) {
.LBB0_1725:
	s_mov_b64 s[2:3], s[88:89]
	s_mov_b32 s4, s38
	s_getreg_b32 s1, hwreg(HW_REG_XCC_ID, 0, 4)
	s_nop 0
	v_mbcnt_lo_u32_b32 v0, s4, 0
	v_mbcnt_hi_u32_b32 v0, s4, v0
	v_add_u32_e32 v0, s93, v0
	s_waitcnt vmcnt(0)
	s_waitcnt lgkmcnt(0)
	v_cmp_eq_u32_e32 vcc, 0, v0
	s_barrier
	s_cmp_lg_u32 s93, 64
	s_cbranch_scc1 .Lbinv_skip_12
	buffer_inv sc1
	s_waitcnt vmcnt(0)

; __device__ __forceinline__ void xcd_barrier(const XcdBarrier& b, bool leader) {
;     ...
;     if (leader) {
.Lbinv_skip_15:
	s_and_saveexec_b64 s[10:11], vcc
	s_cbranch_execnz .LBB0_2081
	s_getpc_b64 s[98:99]
